# speedup vs baseline: 1.0611x; 1.0176x over previous
.LBB0_3:
	s_add_i32 s3, s2, 0xfffffe00
	s_lshr_b32 s8, s3, 3
	s_mul_i32 s9, s8, 0x2493
	s_lshr_b32 s9, s9, 16
	s_mul_i32 s10, s9, 7
	s_sub_u32 s10, s8, s10
	s_cmp_lt_u32 s10, 2
	s_cbranch_scc1 .Lcvt_work
	s_cmp_lt_u32 s9, 32
	s_cbranch_scc0 .LBB0_2
	s_lshl_b32 s9, s9, 3
	s_and_b32 s11, s3, 7
	s_or_b32 s3, s9, s11
	v_cmp_eq_u32_e32 vcc, 0, v0
	v_mov_b32_e32 v1, 0
	s_cmp_eq_u32 s10, 5
	s_cbranch_scc1 .Lcvt_mb_wo
	s_cmp_eq_u32 s10, 4
	s_cbranch_scc1 .Lcvt_mb_kv
	s_cmp_eq_u32 s10, 3
	s_cbranch_scc1 .Lcvt_mb_h2
	s_cmp_eq_u32 s10, 6
	s_cbranch_scc0 .LBB0_2
	s_cmp_eq_u32 s3, 0
	s_cbranch_scc0 .LBB0_2
	s_load_dwordx2 s[6:7], s[0:1], 0x28
	v_mov_b32_e32 v2, 0
	s_waitcnt lgkmcnt(0)
	s_add_u32 s6, s6, 0xa000000
	s_addc_u32 s7, s7, 0
	s_and_saveexec_b64 s[8:9], vcc
	s_cbranch_execz .LBB0_2
	global_store_dword v1, v2, s[6:7]
	global_store_dword v1, v2, s[6:7] offset:64
	s_endpgm

.Lcvt_mb_h2:
	s_load_dwordx2 s[4:5], s[0:1], 0x8
	s_load_dwordx2 s[6:7], s[0:1], 0x0
	s_load_dwordx2 s[14:15], s[0:1], 0x30
	s_lshl_b32 s11, s3, 4
	s_and_b32 s12, s11, 0xffffff8f
	s_and_b32 s13, s11, 0x10
	s_lshl_b32 s13, s13, 2
	s_or_b32 s12, s12, s13
	s_and_b32 s13, s11, 0x60
	s_lshr_b32 s13, s13, 1
	s_or_b32 s12, s12, s13
	s_lshl_b32 s12, s12, 14
	s_add_u32 s12, s12, 0x2000
	s_lshl_b32 s13, s11, 14
	s_add_u32 s13, s13, 0x2000
	s_waitcnt lgkmcnt(0)
	s_add_u32 s4, s4, s12
	s_addc_u32 s5, s5, 0
	s_add_u32 s6, s6, s13
	s_addc_u32 s7, s7, 0
	s_lshl_b32 s13, s11, 13
	s_add_u32 s13, s13, 0x1000
	s_add_u32 s14, s14, s13
	s_addc_u32 s15, s15, 0
	v_mov_b32_e32 v2, s4
	v_mov_b32_e32 v3, s5
	v_mov_b32_e32 v4, s6
	v_mov_b32_e32 v5, s7
	s_and_saveexec_b64 s[8:9], vcc
	s_cbranch_execz .LBB0_2
	global_store_dwordx4 v1, v[2:5], s[14:15]
	s_endpgm

.Lcvt_work:
	s_lshl_b32 s9, s9, 1
	s_add_u32 s9, s9, s10
	s_lshl_b32 s9, s9, 3
	s_and_b32 s10, s3, 7
	s_or_b32 s8, s9, s10
	s_lshl_b32 s8, s8, 1
	s_add_u32 s9, s8, 0x1000
	s_cmp_lt_u32 s8, 0x2000
	s_cselect_b32 s8, s8, s9
	s_load_dwordx4 s[4:7], s[0:1], 0x28
	s_mov_b32 s9, 0
	s_lshl_b64 s[8:9], s[8:9], 8
	v_or_b32_e32 v6, s8, v0
	v_mov_b32_e32 v7, s9
	s_mov_b64 s[8:9], 0x1fffff
	v_cmp_lt_u64_e32 vcc, s[8:9], v[6:7]
	s_mov_b64 s[10:11], 0
	s_and_saveexec_b64 s[8:9], vcc
	s_xor_b64 s[8:9], exec, s[8:9]
	s_cbranch_execnz .LBB0_17
	s_andn2_saveexec_b64 s[8:9], s[8:9]
	s_cbranch_execnz .LBB0_32

.LBB2_56:
	s_lshl_b32 s0, s2, 5
	s_lshr_b32 s1, s2, 3
	s_and_b32 s0, s0, 0x60
	s_lshl_b32 s3, s2, 1
	s_or_b32 s0, s0, s1
	v_lshrrev_b32_e32 v3, 3, v0
	v_bfe_u32 v4, v0, 2, 4
	s_and_b32 s20, s3, 8
	s_bfe_u32 s3, s2, 0x30003
	s_lshr_b32 s21, s0, 3
	v_and_or_b32 v5, v3, 48, v4
	v_or_b32_e32 v3, 64, v3
	s_movk_i32 s0, 0x70
	s_or_b32 s22, s20, s3
	v_and_or_b32 v3, v3, s0, v4
	s_lshl_b32 s0, s21, 21
	s_waitcnt lgkmcnt(0)
	s_lshl_b32 s46, s2, 16
	s_add_u32 s46, s46, 0x2000000
	s_add_u32 s44, s6, s46
	s_addc_u32 s45, s7, 0
	s_load_dwordx2 s[46:47], s[44:45], 0x0
	s_add_u32 s54, s4, 0xa000000
	s_addc_u32 s55, s5, 0
	s_mov_b32 s48, 0
	s_mov_b32 s50, 0
	s_mov_b32 s51, 0
	v_cmp_eq_u32_e64 s[56:57], 0, v0
	v_lshlrev_b32_e32 v226, 5, v0
	v_lshlrev_b32_e32 v227, 4, v0
	s_lshl_b32 s58, s2, 17
	s_add_u32 s58, s58, 0x1000
	s_add_u32 s62, s6, s58
	s_addc_u32 s63, s7, 0
	s_add_u32 s64, s4, s58
	s_addc_u32 s65, s5, 0
	s_load_dwordx4 s[68:71], s[62:63], 0x0
	v_and_b32_e32 v236, 0x100, v0
	v_and_b32_e32 v237, 0xff, v0
	v_lshlrev_b32_e32 v228, 6, v236
	v_lshlrev_b32_e32 v229, 5, v237
	v_lshlrev_b32_e32 v230, 5, v236
	v_lshlrev_b32_e32 v231, 4, v237
	v_or_b32_e32 v236, v228, v229
	v_or_b32_e32 v237, v230, v231
	s_add_u32 s0, s6, s0
	v_lshlrev_b32_e32 v1, 4, v0
	v_and_b32_e32 v2, 32, v0
	s_addc_u32 s1, s7, 0
	s_add_i32 s23, 0, 0x10000
	v_bitop3_b32 v2, v1, v2, 48 bitop3:0x6c
	v_add_u32_e32 v141, s23, v1
	v_and_or_b32 v2, v0, 64, v2
	v_readfirstlane_b32 s6, v141
	v_add_u32_e32 v142, 0x2000, v141
	v_lshl_or_b32 v132, v5, 13, v2
	s_mov_b32 m0, s6
	v_readfirstlane_b32 s6, v142
	global_load_lds_dwordx4 v132, s[0:1]
	s_mov_b32 m0, s6
	s_lshl_b32 s6, s22, 21
	s_add_u32 s6, s4, s6
	s_addc_u32 s7, s5, 0
	v_add_u32_e32 v140, 0, v1
	s_add_u32 s16, s0, 0x100000
	v_lshl_or_b32 v130, v3, 13, v2
	v_readfirstlane_b32 s14, v140
	v_add_u32_e32 v144, 0x2000, v140
	s_addc_u32 s17, s1, 0
	s_add_i32 s24, 0, 0x14000
	global_load_lds_dwordx4 v130, s[0:1]
	s_mov_b32 m0, s14
	v_readfirstlane_b32 s14, v144
	v_add_u32_e32 v145, s24, v1
	global_load_lds_dwordx4 v132, s[6:7]
	s_mov_b32 m0, s14
	v_readfirstlane_b32 s14, v145
	v_add_u32_e32 v146, 0x2000, v145
	global_load_lds_dwordx4 v130, s[6:7]
	s_mov_b32 m0, s14
	v_readfirstlane_b32 s14, v146
	v_add_u32_e32 v148, 0x4000, v140
	global_load_lds_dwordx4 v132, s[16:17]
	s_mov_b32 m0, s14
	s_add_u32 s14, s6, 0x100000
	v_readfirstlane_b32 s18, v148
	v_add_u32_e32 v149, 0x6000, v140
	global_load_lds_dwordx4 v130, s[16:17]
	s_addc_u32 s15, s7, 0
	s_mov_b32 m0, s18
	v_readfirstlane_b32 s18, v149
	global_load_lds_dwordx4 v132, s[14:15]
	s_mov_b32 m0, s18
	v_lshrrev_b32_e32 v2, 8, v0
	global_load_lds_dwordx4 v130, s[14:15]
	v_mov_b32_e32 v133, 0
	v_mov_b32_e32 v131, v133
	v_cmp_eq_u32_e32 vcc, 1, v2
	s_and_saveexec_b64 s[18:19], vcc
	s_cbranch_execz .LBB2_58
	s_barrier

.LBB2_59:
	ds_read_b128 v[160:163], v157
	ds_read_b128 v[164:167], v157 offset:1024
	ds_read_b128 v[168:171], v157 offset:2048
	ds_read_b128 v[172:175], v157 offset:3072
	s_add_u32 s24, s4, s2
	s_addc_u32 s25, s5, s3
	s_add_u32 s24, s24, 0x80
	s_addc_u32 s25, s25, 0
	v_readfirstlane_b32 s26, v158
	v_lshl_add_u64 v[176:177], s[24:25], 0, v[132:133]
	s_mov_b32 m0, s26
	s_nop 0
	global_load_lds_dwordx4 v[176:177], off
	v_lshl_add_u64 v[176:177], s[24:25], 0, v[130:131]
	v_readfirstlane_b32 s24, v159
	s_mov_b32 m0, s24
	s_nop 0
	global_load_lds_dwordx4 v[176:177], off
	ds_read_b128 v[176:179], v138
	ds_read_b128 v[180:183], v138 offset:1024
	ds_read_b128 v[184:187], v137
	ds_read_b128 v[188:191], v137 offset:1024
	ds_read_b128 v[192:195], v136
	ds_read_b128 v[196:199], v136 offset:1024
	ds_read_b128 v[200:203], v135
	ds_read_b128 v[204:207], v135 offset:1024
	s_waitcnt lgkmcnt(8)
	s_barrier
	s_waitcnt lgkmcnt(0)
	s_setprio 1
	s_waitcnt lgkmcnt(0)
	v_mfma_f32_16x16x32_f16 v[126:129], v[160:163], v[176:179], v[126:129]
	v_mfma_f32_16x16x32_f16 v[122:125], v[168:171], v[176:179], v[122:125]
	v_mfma_f32_16x16x32_f16 v[118:121], v[160:163], v[184:187], v[118:121]
	v_mfma_f32_16x16x32_f16 v[114:117], v[168:171], v[184:187], v[114:117]
	v_mfma_f32_16x16x32_f16 v[110:113], v[160:163], v[192:195], v[110:113]
	v_mfma_f32_16x16x32_f16 v[106:109], v[168:171], v[192:195], v[106:109]
	v_mfma_f32_16x16x32_f16 v[102:105], v[160:163], v[200:203], v[102:105]
	v_mfma_f32_16x16x32_f16 v[98:101], v[168:171], v[200:203], v[98:101]
	v_mfma_f32_16x16x32_f16 v[126:129], v[164:167], v[180:183], v[126:129]
	v_mfma_f32_16x16x32_f16 v[122:125], v[172:175], v[180:183], v[122:125]
	v_mfma_f32_16x16x32_f16 v[118:121], v[164:167], v[188:191], v[118:121]
	v_mfma_f32_16x16x32_f16 v[114:117], v[172:175], v[188:191], v[114:117]
	v_mfma_f32_16x16x32_f16 v[110:113], v[164:167], v[196:199], v[110:113]
	v_mfma_f32_16x16x32_f16 v[106:109], v[172:175], v[196:199], v[106:109]
	v_mfma_f32_16x16x32_f16 v[102:105], v[164:167], v[204:207], v[102:105]
	v_mfma_f32_16x16x32_f16 v[98:101], v[172:175], v[204:207], v[98:101]
	s_setprio 0
	s_barrier
	s_add_u32 s26, s0, s2
	s_addc_u32 s27, s1, s3
	s_add_u32 s24, s26, 0x100
	s_addc_u32 s25, s27, 0
	v_readfirstlane_b32 s28, v141
	v_lshl_add_u64 v[224:225], s[24:25], 0, v[132:133]
	s_mov_b32 m0, s28
	ds_read_b128 v[208:211], v153
	ds_read_b128 v[212:215], v153 offset:1024
	ds_read_b128 v[216:219], v153 offset:2048
	ds_read_b128 v[220:223], v153 offset:3072
	global_load_lds_dwordx4 v[224:225], off
	v_lshl_add_u64 v[224:225], s[24:25], 0, v[130:131]
	v_readfirstlane_b32 s24, v142
	s_mov_b32 m0, s24
	s_nop 0
	global_load_lds_dwordx4 v[224:225], off
	s_barrier
	s_waitcnt lgkmcnt(0)
	s_setprio 1
	s_waitcnt lgkmcnt(0)
	v_mfma_f32_16x16x32_f16 v[94:97], v[208:211], v[176:179], v[94:97]
	v_mfma_f32_16x16x32_f16 v[90:93], v[216:219], v[176:179], v[90:93]
	v_mfma_f32_16x16x32_f16 v[86:89], v[208:211], v[184:187], v[86:89]
	v_mfma_f32_16x16x32_f16 v[82:85], v[216:219], v[184:187], v[82:85]
	v_mfma_f32_16x16x32_f16 v[78:81], v[208:211], v[192:195], v[78:81]
	v_mfma_f32_16x16x32_f16 v[74:77], v[216:219], v[192:195], v[74:77]
	v_mfma_f32_16x16x32_f16 v[70:73], v[208:211], v[200:203], v[70:73]
	v_mfma_f32_16x16x32_f16 v[66:69], v[216:219], v[200:203], v[66:69]
	v_mfma_f32_16x16x32_f16 v[94:97], v[212:215], v[180:183], v[94:97]
	v_mfma_f32_16x16x32_f16 v[90:93], v[220:223], v[180:183], v[90:93]
	v_mfma_f32_16x16x32_f16 v[86:89], v[212:215], v[188:191], v[86:89]
	v_mfma_f32_16x16x32_f16 v[82:85], v[220:223], v[188:191], v[82:85]
	v_mfma_f32_16x16x32_f16 v[78:81], v[212:215], v[196:199], v[78:81]
	v_mfma_f32_16x16x32_f16 v[74:77], v[220:223], v[196:199], v[74:77]
	v_mfma_f32_16x16x32_f16 v[70:73], v[212:215], v[204:207], v[70:73]
	v_mfma_f32_16x16x32_f16 v[66:69], v[220:223], v[204:207], v[66:69]
	s_setprio 0
	s_add_u32 s28, s6, s2
	s_addc_u32 s29, s7, s3
	s_add_u32 s24, s28, 0x100
	s_addc_u32 s25, s29, 0
	v_readfirstlane_b32 s30, v140
	v_lshl_add_u64 v[224:225], s[24:25], 0, v[132:133]
	s_mov_b32 m0, s30
	s_barrier
	ds_read_b128 v[176:179], v138 offset:16384
	ds_read_b128 v[180:183], v138 offset:17408
	ds_read_b128 v[184:187], v137 offset:16384
	ds_read_b128 v[188:191], v137 offset:17408
	ds_read_b128 v[192:195], v136 offset:16384
	ds_read_b128 v[196:199], v136 offset:17408
	ds_read_b128 v[200:203], v135 offset:16384
	ds_read_b128 v[204:207], v135 offset:17408
	global_load_lds_dwordx4 v[224:225], off
	v_lshl_add_u64 v[224:225], s[24:25], 0, v[130:131]
	v_readfirstlane_b32 s24, v144
	s_mov_b32 m0, s24
	s_nop 0
	global_load_lds_dwordx4 v[224:225], off
	s_barrier
	s_waitcnt lgkmcnt(0)
	s_setprio 1
	s_waitcnt lgkmcnt(0)
	v_mfma_f32_16x16x32_f16 v[62:65], v[160:163], v[176:179], v[62:65]
	v_mfma_f32_16x16x32_f16 v[58:61], v[168:171], v[176:179], v[58:61]
	v_mfma_f32_16x16x32_f16 v[54:57], v[160:163], v[184:187], v[54:57]
	v_mfma_f32_16x16x32_f16 v[50:53], v[168:171], v[184:187], v[50:53]
	v_mfma_f32_16x16x32_f16 v[46:49], v[160:163], v[192:195], v[46:49]
	v_mfma_f32_16x16x32_f16 v[42:45], v[168:171], v[192:195], v[42:45]
	v_mfma_f32_16x16x32_f16 v[38:41], v[160:163], v[200:203], v[38:41]
	v_mfma_f32_16x16x32_f16 v[34:37], v[168:171], v[200:203], v[34:37]
	v_mfma_f32_16x16x32_f16 v[62:65], v[164:167], v[180:183], v[62:65]
	v_mfma_f32_16x16x32_f16 v[58:61], v[172:175], v[180:183], v[58:61]
	v_mfma_f32_16x16x32_f16 v[54:57], v[164:167], v[188:191], v[54:57]
	v_mfma_f32_16x16x32_f16 v[50:53], v[172:175], v[188:191], v[50:53]
	v_mfma_f32_16x16x32_f16 v[46:49], v[164:167], v[196:199], v[46:49]
	v_mfma_f32_16x16x32_f16 v[42:45], v[172:175], v[196:199], v[42:45]
	v_mfma_f32_16x16x32_f16 v[38:41], v[164:167], v[204:207], v[38:41]
	v_mfma_f32_16x16x32_f16 v[34:37], v[172:175], v[204:207], v[34:37]
	s_setprio 0
	s_barrier
	s_add_u32 s30, s16, s2
	s_addc_u32 s31, s17, s3
	s_add_u32 s24, s30, 0x100
	s_addc_u32 s25, s31, 0
	v_readfirstlane_b32 s33, v145
	v_lshl_add_u64 v[160:161], s[24:25], 0, v[132:133]
	s_mov_b32 m0, s33
	s_nop 0
	global_load_lds_dwordx4 v[160:161], off
	v_lshl_add_u64 v[160:161], s[24:25], 0, v[130:131]
	v_readfirstlane_b32 s24, v146
	s_mov_b32 m0, s24
	s_nop 0
	global_load_lds_dwordx4 v[160:161], off
	s_mov_b32 s49, s48
	s_add_i32 s48, s48, 1
	s_cmp_gt_u32 s49, 20
	s_cbranch_scc1 .Ls1_plain
	s_cmp_eq_u32 s49, 0
	s_cbranch_scc1 .Ls1_h0
	s_cmp_lt_u32 s49, 8
	s_cbranch_scc1 .Ls1_hm
	s_cmp_eq_u32 s49, 8
	s_cbranch_scc1 .Ls1_hl
	s_cmp_eq_u32 s49, 10
	s_cbranch_scc1 .Ls1_arr
	s_cmp_eq_u32 s49, 12
	s_cbranch_scc1 .Ls1_k0
	s_cmp_lt_u32 s49, 12
	s_cbranch_scc1 .Ls1_plain
	s_cmp_lt_u32 s49, 20
	s_cbranch_scc1 .Ls1_km
	s_mov_b32 s59, 7
	s_waitcnt vmcnt(16)
	v_cvt_pk_f16_f32 v228, v228, v229
	v_cvt_pk_f16_f32 v229, v230, v231
	v_cvt_pk_f16_f32 v230, v232, v233
	v_cvt_pk_f16_f32 v231, v234, v235
	s_lshl_b32 s58, s59, 13
	s_add_u32 s52, s44, s58
	s_addc_u32 s53, s45, 0
	global_store_dwordx4 v227, v[228:231], s[52:53] sc1
	s_waitcnt vmcnt(7)
	s_branch .Ls1_join

.Ls1_h0:
	s_mov_b32 s59, 0
	s_cmp_lt_u32 s59, 8
	s_cselect_b32 s52, s68, s70
	s_cselect_b32 s53, s69, s71
	s_and_b32 s58, s59, 7
	s_lshl_b32 s58, s58, 15
	s_add_u32 s52, s52, s58
	s_addc_u32 s53, s53, 0
	global_load_dwordx4 v[228:231], v236, s[52:53] nt
	global_load_dwordx4 v[232:235], v236, s[52:53] offset:16 nt
	s_waitcnt vmcnt(8)
	s_branch .Ls1_join
.Ls1_hm:
	s_lshl_b32 s59, s49, 1
	s_sub_u32 s59, s59, 1
	s_waitcnt vmcnt(8)
	v_cvt_pk_f16_f32 v228, v228, v229
	v_cvt_pk_f16_f32 v229, v230, v231
	v_cvt_pk_f16_f32 v230, v232, v233
	v_cvt_pk_f16_f32 v231, v234, v235
	s_cmp_lt_u32 s59, 8
	s_cselect_b32 s52, s62, s64
	s_cselect_b32 s53, s63, s65
	s_and_b32 s58, s59, 7
	s_lshl_b32 s58, s58, 14
	s_add_u32 s52, s52, s58
	s_addc_u32 s53, s53, 0
	global_store_dwordx4 v237, v[228:231], s[52:53] sc1
	s_add_u32 s59, s59, 1
	s_cmp_lt_u32 s59, 8
	s_cselect_b32 s52, s68, s70
	s_cselect_b32 s53, s69, s71
	s_and_b32 s58, s59, 7
	s_lshl_b32 s58, s58, 15
	s_add_u32 s52, s52, s58
	s_addc_u32 s53, s53, 0
	global_load_dwordx4 v[228:231], v236, s[52:53] nt
	global_load_dwordx4 v[232:235], v236, s[52:53] offset:16 nt
	s_waitcnt vmcnt(9)
	s_branch .Ls1_join
.Ls1_hl:
	s_mov_b32 s59, 15
	s_waitcnt vmcnt(8)
	v_cvt_pk_f16_f32 v228, v228, v229
	v_cvt_pk_f16_f32 v229, v230, v231
	v_cvt_pk_f16_f32 v230, v232, v233
	v_cvt_pk_f16_f32 v231, v234, v235
	s_cmp_lt_u32 s59, 8
	s_cselect_b32 s52, s62, s64
	s_cselect_b32 s53, s63, s65
	s_and_b32 s58, s59, 7
	s_lshl_b32 s58, s58, 14
	s_add_u32 s52, s52, s58
	s_addc_u32 s53, s53, 0
	global_store_dwordx4 v237, v[228:231], s[52:53] sc1
	s_waitcnt vmcnt(7)
	s_branch .Ls1_join
.Ls1_arr:
	s_and_saveexec_b64 s[52:53], s[56:57]
	s_cbranch_execz .Ls1_arr_no
	v_mov_b32_e32 v228, 0
	v_mov_b32_e32 v229, 1
	global_atomic_add v228, v229, s[54:55] offset:64 sc1
	s_or_b64 exec, exec, s[52:53]
	s_waitcnt vmcnt(7)
	s_branch .Ls1_join
.Ls1_arr_no:
	s_or_b64 exec, exec, s[52:53]
	s_waitcnt vmcnt(6)
	s_branch .Ls1_join
.Ls1_k0:
	s_cmp_eq_u64 s[56:57], 0
	s_cbranch_scc1 .Ls1_k0_go
	s_mov_b32 s58, 0
	v_mov_b32_e32 v234, 0
.Ls1_poll:
	global_load_dword v235, v234, s[54:55] offset:64 sc1
	s_waitcnt vmcnt(0)
	v_readfirstlane_b32 s59, v235
	s_cmp_ge_u32 s59, 0x100
	s_cbranch_scc1 .Ls1_k0_go
	s_add_i32 s58, s58, 1
	s_cmp_lt_u32 s58, 0x190
	s_cbranch_scc0 .Ls1_k0_go
	s_sleep 4
	s_branch .Ls1_poll
.Ls1_k0_go:
	s_mov_b32 s59, 0
	s_lshl_b32 s58, s59, 14
	s_add_u32 s52, s46, s58
	s_addc_u32 s53, s47, 0
	global_load_dwordx4 v[228:231], v226, s[52:53] nt
	global_load_dwordx4 v[232:235], v226, s[52:53] offset:16 nt
	s_waitcnt vmcnt(8)
	s_branch .Ls1_join
.Ls1_km:
	s_sub_u32 s59, s49, 13
	s_waitcnt vmcnt(16)
	v_cvt_pk_f16_f32 v228, v228, v229
	v_cvt_pk_f16_f32 v229, v230, v231
	v_cvt_pk_f16_f32 v230, v232, v233
	v_cvt_pk_f16_f32 v231, v234, v235
	s_lshl_b32 s58, s59, 13
	s_add_u32 s52, s44, s58
	s_addc_u32 s53, s45, 0
	global_store_dwordx4 v227, v[228:231], s[52:53] sc1
	s_add_u32 s59, s59, 1
	s_lshl_b32 s58, s59, 14
	s_add_u32 s52, s46, s58
	s_addc_u32 s53, s47, 0
	global_load_dwordx4 v[228:231], v226, s[52:53] nt
	global_load_dwordx4 v[232:235], v226, s[52:53] offset:16 nt
	s_waitcnt vmcnt(9)
.Ls1_join:
	s_barrier
	s_setprio 1
	v_mfma_f32_16x16x32_f16 v[30:33], v[208:211], v[176:179], v[30:33]
	v_mfma_f32_16x16x32_f16 v[26:29], v[216:219], v[176:179], v[26:29]
	v_mfma_f32_16x16x32_f16 v[22:25], v[208:211], v[184:187], v[22:25]
	v_mfma_f32_16x16x32_f16 v[18:21], v[216:219], v[184:187], v[18:21]
	v_mfma_f32_16x16x32_f16 v[14:17], v[208:211], v[192:195], v[14:17]
	v_mfma_f32_16x16x32_f16 v[10:13], v[216:219], v[192:195], v[10:13]
	v_mfma_f32_16x16x32_f16 v[6:9], v[208:211], v[200:203], v[6:9]
	v_mfma_f32_16x16x32_f16 v[2:5], v[216:219], v[200:203], v[2:5]
	v_mfma_f32_16x16x32_f16 v[30:33], v[212:215], v[180:183], v[30:33]
	v_mfma_f32_16x16x32_f16 v[26:29], v[220:223], v[180:183], v[26:29]
	v_mfma_f32_16x16x32_f16 v[22:25], v[212:215], v[188:191], v[22:25]
	v_mfma_f32_16x16x32_f16 v[18:21], v[220:223], v[188:191], v[18:21]
	v_mfma_f32_16x16x32_f16 v[14:17], v[212:215], v[196:199], v[14:17]
	v_mfma_f32_16x16x32_f16 v[10:13], v[220:223], v[196:199], v[10:13]
	v_mfma_f32_16x16x32_f16 v[6:9], v[212:215], v[204:207], v[6:9]
	v_mfma_f32_16x16x32_f16 v[2:5], v[220:223], v[204:207], v[2:5]
	s_setprio 0
	s_barrier
	ds_read_b128 v[160:163], v143
	ds_read_b128 v[164:167], v143 offset:1024
	ds_read_b128 v[168:171], v143 offset:2048
	ds_read_b128 v[172:175], v143 offset:3072
	s_add_u32 s24, s18, s2
	s_addc_u32 s25, s19, s3
	v_readfirstlane_b32 s33, v148
	v_lshl_add_u64 v[208:209], s[24:25], 0, v[132:133]
	s_mov_b32 m0, s33
	ds_read_b128 v[176:179], v138 offset:32768
	ds_read_b128 v[180:183], v138 offset:33792
	ds_read_b128 v[184:187], v137 offset:32768
	ds_read_b128 v[188:191], v137 offset:33792
	ds_read_b128 v[192:195], v136 offset:32768
	ds_read_b128 v[196:199], v136 offset:33792
	ds_read_b128 v[200:203], v135 offset:32768
	ds_read_b128 v[204:207], v135 offset:33792
	global_load_lds_dwordx4 v[208:209], off
	v_lshl_add_u64 v[208:209], s[24:25], 0, v[130:131]
	v_readfirstlane_b32 s24, v149
	s_mov_b32 m0, s24
	s_nop 0
	global_load_lds_dwordx4 v[208:209], off
	s_waitcnt lgkmcnt(8)
	s_barrier
	s_waitcnt lgkmcnt(0)
	s_setprio 1
	s_waitcnt lgkmcnt(0)
	v_mfma_f32_16x16x32_f16 v[126:129], v[160:163], v[176:179], v[126:129]
	v_mfma_f32_16x16x32_f16 v[122:125], v[168:171], v[176:179], v[122:125]
	v_mfma_f32_16x16x32_f16 v[118:121], v[160:163], v[184:187], v[118:121]
	v_mfma_f32_16x16x32_f16 v[114:117], v[168:171], v[184:187], v[114:117]
	v_mfma_f32_16x16x32_f16 v[110:113], v[160:163], v[192:195], v[110:113]
	v_mfma_f32_16x16x32_f16 v[106:109], v[168:171], v[192:195], v[106:109]
	v_mfma_f32_16x16x32_f16 v[102:105], v[160:163], v[200:203], v[102:105]
	v_mfma_f32_16x16x32_f16 v[98:101], v[168:171], v[200:203], v[98:101]
	v_mfma_f32_16x16x32_f16 v[126:129], v[164:167], v[180:183], v[126:129]
	v_mfma_f32_16x16x32_f16 v[122:125], v[172:175], v[180:183], v[122:125]
	v_mfma_f32_16x16x32_f16 v[118:121], v[164:167], v[188:191], v[118:121]
	v_mfma_f32_16x16x32_f16 v[114:117], v[172:175], v[188:191], v[114:117]
	v_mfma_f32_16x16x32_f16 v[110:113], v[164:167], v[196:199], v[110:113]
	v_mfma_f32_16x16x32_f16 v[106:109], v[172:175], v[196:199], v[106:109]
	v_mfma_f32_16x16x32_f16 v[102:105], v[164:167], v[204:207], v[102:105]
	v_mfma_f32_16x16x32_f16 v[98:101], v[172:175], v[204:207], v[98:101]
	s_setprio 0
	s_barrier
	s_add_u32 s24, s26, 0x180
	s_addc_u32 s25, s27, 0
	v_readfirstlane_b32 s26, v150
	v_lshl_add_u64 v[224:225], s[24:25], 0, v[132:133]
	s_mov_b32 m0, s26
	ds_read_b128 v[208:211], v139
	ds_read_b128 v[212:215], v139 offset:1024
	ds_read_b128 v[216:219], v139 offset:2048
	ds_read_b128 v[220:223], v139 offset:3072
	global_load_lds_dwordx4 v[224:225], off
	v_lshl_add_u64 v[224:225], s[24:25], 0, v[130:131]
	v_readfirstlane_b32 s24, v151
	s_mov_b32 m0, s24
	s_nop 0
	global_load_lds_dwordx4 v[224:225], off
	s_barrier
	s_waitcnt lgkmcnt(0)
	s_setprio 1
	s_waitcnt lgkmcnt(0)
	v_mfma_f32_16x16x32_f16 v[94:97], v[208:211], v[176:179], v[94:97]
	v_mfma_f32_16x16x32_f16 v[90:93], v[216:219], v[176:179], v[90:93]
	v_mfma_f32_16x16x32_f16 v[86:89], v[208:211], v[184:187], v[86:89]
	v_mfma_f32_16x16x32_f16 v[82:85], v[216:219], v[184:187], v[82:85]
	v_mfma_f32_16x16x32_f16 v[78:81], v[208:211], v[192:195], v[78:81]
	v_mfma_f32_16x16x32_f16 v[74:77], v[216:219], v[192:195], v[74:77]
	v_mfma_f32_16x16x32_f16 v[70:73], v[208:211], v[200:203], v[70:73]
	v_mfma_f32_16x16x32_f16 v[66:69], v[216:219], v[200:203], v[66:69]
	v_mfma_f32_16x16x32_f16 v[94:97], v[212:215], v[180:183], v[94:97]
	v_mfma_f32_16x16x32_f16 v[90:93], v[220:223], v[180:183], v[90:93]
	v_mfma_f32_16x16x32_f16 v[86:89], v[212:215], v[188:191], v[86:89]
	v_mfma_f32_16x16x32_f16 v[82:85], v[220:223], v[188:191], v[82:85]
	v_mfma_f32_16x16x32_f16 v[78:81], v[212:215], v[196:199], v[78:81]
	v_mfma_f32_16x16x32_f16 v[74:77], v[220:223], v[196:199], v[74:77]
	v_mfma_f32_16x16x32_f16 v[70:73], v[212:215], v[204:207], v[70:73]
	v_mfma_f32_16x16x32_f16 v[66:69], v[220:223], v[204:207], v[66:69]
	s_setprio 0
	s_add_u32 s24, s28, 0x180
	s_addc_u32 s25, s29, 0
	v_readfirstlane_b32 s26, v152
	v_lshl_add_u64 v[224:225], s[24:25], 0, v[132:133]
	s_mov_b32 m0, s26
	s_barrier
	ds_read_b128 v[176:179], v138 offset:49152
	ds_read_b128 v[180:183], v138 offset:50176
	ds_read_b128 v[184:187], v137 offset:49152
	ds_read_b128 v[188:191], v137 offset:50176
	ds_read_b128 v[192:195], v136 offset:49152
	ds_read_b128 v[196:199], v136 offset:50176
	ds_read_b128 v[200:203], v135 offset:49152
	ds_read_b128 v[204:207], v135 offset:50176
	global_load_lds_dwordx4 v[224:225], off
	v_lshl_add_u64 v[224:225], s[24:25], 0, v[130:131]
	v_readfirstlane_b32 s24, v154
	s_mov_b32 m0, s24
	s_nop 0
	global_load_lds_dwordx4 v[224:225], off
	s_barrier
	s_waitcnt lgkmcnt(0)
	s_setprio 1
	s_waitcnt lgkmcnt(0)
	v_mfma_f32_16x16x32_f16 v[62:65], v[160:163], v[176:179], v[62:65]
	v_mfma_f32_16x16x32_f16 v[58:61], v[168:171], v[176:179], v[58:61]
	v_mfma_f32_16x16x32_f16 v[54:57], v[160:163], v[184:187], v[54:57]
	v_mfma_f32_16x16x32_f16 v[50:53], v[168:171], v[184:187], v[50:53]
	v_mfma_f32_16x16x32_f16 v[46:49], v[160:163], v[192:195], v[46:49]
	v_mfma_f32_16x16x32_f16 v[42:45], v[168:171], v[192:195], v[42:45]
	v_mfma_f32_16x16x32_f16 v[38:41], v[160:163], v[200:203], v[38:41]
	v_mfma_f32_16x16x32_f16 v[34:37], v[168:171], v[200:203], v[34:37]
	v_mfma_f32_16x16x32_f16 v[62:65], v[164:167], v[180:183], v[62:65]
	v_mfma_f32_16x16x32_f16 v[58:61], v[172:175], v[180:183], v[58:61]
	v_mfma_f32_16x16x32_f16 v[54:57], v[164:167], v[188:191], v[54:57]
	v_mfma_f32_16x16x32_f16 v[50:53], v[172:175], v[188:191], v[50:53]
	v_mfma_f32_16x16x32_f16 v[46:49], v[164:167], v[196:199], v[46:49]
	v_mfma_f32_16x16x32_f16 v[42:45], v[172:175], v[196:199], v[42:45]
	v_mfma_f32_16x16x32_f16 v[38:41], v[164:167], v[204:207], v[38:41]
	v_mfma_f32_16x16x32_f16 v[34:37], v[172:175], v[204:207], v[34:37]
	s_setprio 0
	s_barrier
	s_add_u32 s24, s30, 0x180
	s_addc_u32 s25, s31, 0
	v_readfirstlane_b32 s26, v155
	v_lshl_add_u64 v[160:161], s[24:25], 0, v[132:133]
	s_mov_b32 m0, s26
	s_nop 0
	global_load_lds_dwordx4 v[160:161], off
	v_lshl_add_u64 v[160:161], s[24:25], 0, v[130:131]
	v_readfirstlane_b32 s24, v156
	s_mov_b32 m0, s24
	s_nop 0
	global_load_lds_dwordx4 v[160:161], off
	s_cmp_lt_u32 s49, 8
	s_cbranch_scc1 .Ls2_hm
	s_waitcnt vmcnt(6)
	s_branch .Ls2_join
.Ls2_hm:
	s_lshl_b32 s59, s49, 1
	s_waitcnt vmcnt(8)
	v_cvt_pk_f16_f32 v228, v228, v229
	v_cvt_pk_f16_f32 v229, v230, v231
	v_cvt_pk_f16_f32 v230, v232, v233
	v_cvt_pk_f16_f32 v231, v234, v235
	s_cmp_lt_u32 s59, 8
	s_cselect_b32 s52, s62, s64
	s_cselect_b32 s53, s63, s65
	s_and_b32 s58, s59, 7
	s_lshl_b32 s58, s58, 14
	s_add_u32 s52, s52, s58
	s_addc_u32 s53, s53, 0
	global_store_dwordx4 v237, v[228:231], s[52:53] sc1
	s_add_u32 s59, s59, 1
	s_cmp_lt_u32 s59, 8
	s_cselect_b32 s52, s68, s70
	s_cselect_b32 s53, s69, s71
	s_and_b32 s58, s59, 7
	s_lshl_b32 s58, s58, 15
	s_add_u32 s52, s52, s58
	s_addc_u32 s53, s53, 0
	global_load_dwordx4 v[228:231], v236, s[52:53] nt
	global_load_dwordx4 v[232:235], v236, s[52:53] offset:16 nt
	s_waitcnt vmcnt(9)
.Ls2_join:
	s_barrier
	s_setprio 1
	v_mfma_f32_16x16x32_f16 v[30:33], v[208:211], v[176:179], v[30:33]
	v_mfma_f32_16x16x32_f16 v[26:29], v[216:219], v[176:179], v[26:29]
	v_mfma_f32_16x16x32_f16 v[22:25], v[208:211], v[184:187], v[22:25]
	v_mfma_f32_16x16x32_f16 v[18:21], v[216:219], v[184:187], v[18:21]
	v_mfma_f32_16x16x32_f16 v[14:17], v[208:211], v[192:195], v[14:17]
	v_mfma_f32_16x16x32_f16 v[10:13], v[216:219], v[192:195], v[10:13]
	v_mfma_f32_16x16x32_f16 v[6:9], v[208:211], v[200:203], v[6:9]
	v_mfma_f32_16x16x32_f16 v[2:5], v[216:219], v[200:203], v[2:5]
	v_mfma_f32_16x16x32_f16 v[30:33], v[212:215], v[180:183], v[30:33]
	v_mfma_f32_16x16x32_f16 v[26:29], v[220:223], v[180:183], v[26:29]
	v_mfma_f32_16x16x32_f16 v[22:25], v[212:215], v[188:191], v[22:25]
	v_mfma_f32_16x16x32_f16 v[18:21], v[220:223], v[188:191], v[18:21]
	v_mfma_f32_16x16x32_f16 v[14:17], v[212:215], v[196:199], v[14:17]
	v_mfma_f32_16x16x32_f16 v[10:13], v[220:223], v[196:199], v[10:13]
	v_mfma_f32_16x16x32_f16 v[6:9], v[212:215], v[204:207], v[6:9]
	v_mfma_f32_16x16x32_f16 v[2:5], v[220:223], v[204:207], v[2:5]
	s_setprio 0
	s_add_i32 s23, s23, 2
	s_add_u32 s2, s2, 0x100
	s_addc_u32 s3, s3, 0
	s_cmp_lt_u32 s23, 60
	s_barrier
	s_cbranch_scc1 .LBB2_59
	s_add_u32 s0, s14, 0x1f80
	v_add_u32_e32 v141, 0xc000, v140
	s_addc_u32 s1, s15, 0
	v_readfirstlane_b32 s2, v141
	v_lshl_add_u64 v[132:133], s[0:1], 0, v[132:133]
	s_mov_b32 m0, s2
	ds_read_b128 v[148:151], v157
	ds_read_b128 v[158:161], v157 offset:1024
	ds_read_b128 v[162:165], v157 offset:2048
	ds_read_b128 v[154:157], v157 offset:3072
	global_load_lds_dwordx4 v[132:133], off
	v_add_u32_e32 v132, 0xe000, v140
	v_lshl_add_u64 v[130:131], s[0:1], 0, v[130:131]
	v_readfirstlane_b32 s0, v132
	s_mov_b32 m0, s0
	s_nop 0
	global_load_lds_dwordx4 v[130:131], off
	ds_read_b128 v[130:133], v138
	ds_read_b128 v[166:169], v138 offset:1024
	ds_read_b128 v[170:173], v137
	ds_read_b128 v[174:177], v137 offset:1024
	ds_read_b128 v[178:181], v136
	ds_read_b128 v[182:185], v136 offset:1024
	ds_read_b128 v[186:189], v135
	ds_read_b128 v[190:193], v135 offset:1024
	s_barrier
	s_waitcnt lgkmcnt(0)
	s_setprio 1
	s_waitcnt lgkmcnt(0)
	v_mfma_f32_16x16x32_f16 v[126:129], v[148:151], v[130:133], v[126:129]
	v_mfma_f32_16x16x32_f16 v[122:125], v[162:165], v[130:133], v[122:125]
	v_mfma_f32_16x16x32_f16 v[118:121], v[148:151], v[170:173], v[118:121]
	v_mfma_f32_16x16x32_f16 v[114:117], v[162:165], v[170:173], v[114:117]
	v_mfma_f32_16x16x32_f16 v[110:113], v[148:151], v[178:181], v[110:113]
	v_mfma_f32_16x16x32_f16 v[106:109], v[162:165], v[178:181], v[106:109]
	v_mfma_f32_16x16x32_f16 v[102:105], v[148:151], v[186:189], v[102:105]
	v_mfma_f32_16x16x32_f16 v[126:129], v[158:161], v[166:169], v[126:129]
	v_mfma_f32_16x16x32_f16 v[122:125], v[154:157], v[166:169], v[122:125]
	v_mfma_f32_16x16x32_f16 v[118:121], v[158:161], v[174:177], v[118:121]
	v_mfma_f32_16x16x32_f16 v[114:117], v[154:157], v[174:177], v[114:117]
	v_mfma_f32_16x16x32_f16 v[110:113], v[158:161], v[182:185], v[110:113]
	v_mfma_f32_16x16x32_f16 v[106:109], v[154:157], v[182:185], v[106:109]
	v_mfma_f32_16x16x32_f16 v[102:105], v[158:161], v[190:193], v[102:105]
	v_mfma_f32_16x16x32_f16 v[98:101], v[162:165], v[186:189], v[98:101]
	v_mfma_f32_16x16x32_f16 v[194:197], v[154:157], v[190:193], v[98:101]
	s_setprio 0
	s_barrier
	s_nop 4
	ds_read_b128 v[98:101], v153
	ds_read_b128 v[198:201], v153 offset:1024
	ds_read_b128 v[202:205], v153 offset:2048
	ds_read_b128 v[206:209], v153 offset:3072
	s_barrier
	s_waitcnt lgkmcnt(0)
	s_setprio 1
	s_waitcnt lgkmcnt(0)
	v_mfma_f32_16x16x32_f16 v[82:85], v[202:205], v[170:173], v[82:85]
	v_mfma_f32_16x16x32_f16 v[78:81], v[98:101], v[178:181], v[78:81]
	v_mfma_f32_16x16x32_f16 v[74:77], v[202:205], v[178:181], v[74:77]
	v_mfma_f32_16x16x32_f16 v[70:73], v[98:101], v[186:189], v[70:73]
	v_mfma_f32_16x16x32_f16 v[94:97], v[98:101], v[130:133], v[94:97]
	v_mfma_f32_16x16x32_f16 v[90:93], v[202:205], v[130:133], v[90:93]
	v_mfma_f32_16x16x32_f16 v[86:89], v[98:101], v[170:173], v[86:89]
	v_mfma_f32_16x16x32_f16 v[82:85], v[206:209], v[174:177], v[82:85]
	v_mfma_f32_16x16x32_f16 v[78:81], v[198:201], v[182:185], v[78:81]
	v_mfma_f32_16x16x32_f16 v[74:77], v[206:209], v[182:185], v[74:77]
	v_mfma_f32_16x16x32_f16 v[70:73], v[198:201], v[190:193], v[70:73]
	v_mfma_f32_16x16x32_f16 v[66:69], v[202:205], v[186:189], v[66:69]
	v_mfma_f32_16x16x32_f16 v[210:213], v[198:201], v[166:169], v[94:97]
	v_mfma_f32_16x16x32_f16 v[166:169], v[206:209], v[166:169], v[90:93]
	v_mfma_f32_16x16x32_f16 v[214:217], v[198:201], v[174:177], v[86:89]
	v_mfma_f32_16x16x32_f16 v[66:69], v[206:209], v[190:193], v[66:69]
	s_setprio 0
	s_barrier
	ds_read_b128 v[86:89], v138 offset:16384
	ds_read_b128 v[90:93], v138 offset:17408
	ds_read_b128 v[94:97], v137 offset:16384
	ds_read_b128 v[130:133], v137 offset:17408
	ds_read_b128 v[170:173], v136 offset:16384
	ds_read_b128 v[174:177], v136 offset:17408
	ds_read_b128 v[178:181], v135 offset:16384
	ds_read_b128 v[182:185], v135 offset:17408
	s_waitcnt vmcnt(4)
	s_barrier
	s_waitcnt lgkmcnt(0)
	s_setprio 1
	s_waitcnt lgkmcnt(0)
	v_mfma_f32_16x16x32_f16 v[62:65], v[148:151], v[86:89], v[62:65]
	v_mfma_f32_16x16x32_f16 v[54:57], v[148:151], v[94:97], v[54:57]
	v_mfma_f32_16x16x32_f16 v[46:49], v[148:151], v[170:173], v[46:49]
	v_mfma_f32_16x16x32_f16 v[42:45], v[162:165], v[170:173], v[42:45]
	v_mfma_f32_16x16x32_f16 v[38:41], v[148:151], v[178:181], v[38:41]
	v_mfma_f32_16x16x32_f16 v[34:37], v[162:165], v[178:181], v[34:37]
	v_mfma_f32_16x16x32_f16 v[62:65], v[158:161], v[90:93], v[62:65]
	v_mfma_f32_16x16x32_f16 v[58:61], v[162:165], v[86:89], v[58:61]
	v_mfma_f32_16x16x32_f16 v[54:57], v[158:161], v[130:133], v[54:57]
	v_mfma_f32_16x16x32_f16 v[50:53], v[162:165], v[94:97], v[50:53]
	v_mfma_f32_16x16x32_f16 v[46:49], v[158:161], v[174:177], v[46:49]
	v_mfma_f32_16x16x32_f16 v[42:45], v[154:157], v[174:177], v[42:45]
	v_mfma_f32_16x16x32_f16 v[38:41], v[158:161], v[182:185], v[38:41]
	v_mfma_f32_16x16x32_f16 v[34:37], v[154:157], v[182:185], v[34:37]
	v_mfma_f32_16x16x32_f16 v[186:189], v[154:157], v[90:93], v[58:61]
	v_mfma_f32_16x16x32_f16 v[190:193], v[154:157], v[130:133], v[50:53]
	s_setprio 0
	s_setprio 1
	v_mfma_f32_16x16x32_f16 v[14:17], v[98:101], v[170:173], v[14:17]
	v_mfma_f32_16x16x32_f16 v[6:9], v[98:101], v[178:181], v[6:9]
	v_mfma_f32_16x16x32_f16 v[30:33], v[98:101], v[86:89], v[30:33]
	v_mfma_f32_16x16x32_f16 v[26:29], v[202:205], v[86:89], v[26:29]
	v_mfma_f32_16x16x32_f16 v[22:25], v[98:101], v[94:97], v[22:25]
	v_mfma_f32_16x16x32_f16 v[18:21], v[202:205], v[94:97], v[18:21]
	v_mfma_f32_16x16x32_f16 v[14:17], v[198:201], v[174:177], v[14:17]
	v_mfma_f32_16x16x32_f16 v[10:13], v[202:205], v[170:173], v[10:13]
	v_mfma_f32_16x16x32_f16 v[6:9], v[198:201], v[182:185], v[6:9]
	v_mfma_f32_16x16x32_f16 v[2:5], v[202:205], v[178:181], v[2:5]
	v_mfma_f32_16x16x32_f16 v[148:151], v[198:201], v[90:93], v[30:33]
	v_mfma_f32_16x16x32_f16 v[152:155], v[206:209], v[90:93], v[26:29]
	v_mfma_f32_16x16x32_f16 v[156:159], v[198:201], v[130:133], v[22:25]
	v_mfma_f32_16x16x32_f16 v[160:163], v[206:209], v[130:133], v[18:21]
	v_mfma_f32_16x16x32_f16 v[170:173], v[206:209], v[174:177], v[10:13]
	v_mfma_f32_16x16x32_f16 v[174:177], v[206:209], v[182:185], v[2:5]
	s_setprio 0
	s_barrier
	s_nop 0
	ds_read_b128 v[2:5], v143
	ds_read_b128 v[10:13], v143 offset:1024
	ds_read_b128 v[22:25], v143 offset:2048
	ds_read_b128 v[140:143], v143 offset:3072
	ds_read_b128 v[18:21], v138 offset:32768
	ds_read_b128 v[26:29], v138 offset:33792
	ds_read_b128 v[30:33], v137 offset:32768
	ds_read_b128 v[50:53], v137 offset:33792
	ds_read_b128 v[58:61], v136 offset:32768
	ds_read_b128 v[178:181], v136 offset:33792
	ds_read_b128 v[182:185], v135 offset:32768
	ds_read_b128 v[198:201], v135 offset:33792
	s_waitcnt vmcnt(2)
	s_barrier
	s_waitcnt lgkmcnt(0)
	s_setprio 1
	s_waitcnt lgkmcnt(0)
	v_mfma_f32_16x16x32_f16 v[86:89], v[2:5], v[18:21], v[126:129]
	v_mfma_f32_16x16x32_f16 v[126:129], v[10:13], v[26:29], v[86:89]
	v_mfma_f32_16x16x32_f16 v[86:89], v[22:25], v[18:21], v[122:125]
	v_mfma_f32_16x16x32_f16 v[130:133], v[140:143], v[26:29], v[86:89]
	v_mfma_f32_16x16x32_f16 v[86:89], v[2:5], v[30:33], v[118:121]
	v_mfma_f32_16x16x32_f16 v[118:121], v[10:13], v[50:53], v[86:89]
	v_mfma_f32_16x16x32_f16 v[86:89], v[22:25], v[30:33], v[114:117]
	v_mfma_f32_16x16x32_f16 v[122:125], v[140:143], v[50:53], v[86:89]
	v_mfma_f32_16x16x32_f16 v[86:89], v[2:5], v[58:61], v[110:113]
	v_mfma_f32_16x16x32_f16 v[94:97], v[10:13], v[178:181], v[86:89]
	v_mfma_f32_16x16x32_f16 v[86:89], v[22:25], v[58:61], v[106:109]
	v_mfma_f32_16x16x32_f16 v[98:101], v[140:143], v[178:181], v[86:89]
	v_mfma_f32_16x16x32_f16 v[86:89], v[2:5], v[182:185], v[102:105]
	v_mfma_f32_16x16x32_f16 v[90:93], v[22:25], v[182:185], v[194:197]
	v_mfma_f32_16x16x32_f16 v[86:89], v[10:13], v[198:201], v[86:89]
	v_mfma_f32_16x16x32_f16 v[90:93], v[140:143], v[198:201], v[90:93]
	s_setprio 0
	s_barrier
	ds_read_b128 v[194:197], v139
	ds_read_b128 v[202:205], v139 offset:1024
	ds_read_b128 v[206:209], v139 offset:2048
	ds_read_b128 v[218:221], v139 offset:3072
	s_waitcnt vmcnt(0)
	s_barrier
	s_and_saveexec_b64 s[52:53], s[56:57]
	s_cbranch_execz .Lkv_noarrive
	v_mov_b32_e32 v228, 0
	v_mov_b32_e32 v229, 1
	global_atomic_add v228, v229, s[54:55] sc1

	.amdhsa_kernel _Z15gemm_qkv_kernelPKDF16_S0_PDF16_PKfS3_PK15HIP_vector_typeIfLj2EE
		.amdhsa_group_segment_fixed_size 0
		.amdhsa_private_segment_fixed_size 0
		.amdhsa_kernarg_size 48
		.amdhsa_user_sgpr_count 2
		.amdhsa_user_sgpr_dispatch_ptr 0
		.amdhsa_user_sgpr_queue_ptr 0
		.amdhsa_user_sgpr_kernarg_segment_ptr 1
		.amdhsa_user_sgpr_dispatch_id 0
		.amdhsa_user_sgpr_kernarg_preload_length 0
		.amdhsa_user_sgpr_kernarg_preload_offset 0
		.amdhsa_user_sgpr_private_segment_size 0
		.amdhsa_uses_dynamic_stack 0
		.amdhsa_enable_private_segment 0
		.amdhsa_system_sgpr_workgroup_id_x 1
		.amdhsa_system_sgpr_workgroup_id_y 0
		.amdhsa_system_sgpr_workgroup_id_z 0
		.amdhsa_system_sgpr_workgroup_info 0
		.amdhsa_system_vgpr_workitem_id 0
		.amdhsa_next_free_vgpr 240
		.amdhsa_next_free_sgpr 72
		.amdhsa_accum_offset 240
		.amdhsa_reserve_vcc 1
		.amdhsa_float_round_mode_32 0
		.amdhsa_float_round_mode_16_64 0
		.amdhsa_float_denorm_mode_32 3
		.amdhsa_float_denorm_mode_16_64 3
		.amdhsa_dx10_clamp 1
		.amdhsa_ieee_mode 1
		.amdhsa_fp16_overflow 0
		.amdhsa_tg_split 0
		.amdhsa_exception_fp_ieee_invalid_op 0
		.amdhsa_exception_fp_denorm_src 0
		.amdhsa_exception_fp_ieee_div_zero 0
		.amdhsa_exception_fp_ieee_overflow 0
		.amdhsa_exception_fp_ieee_underflow 0
		.amdhsa_exception_fp_ieee_inexact 0
		.amdhsa_exception_int_div_zero 0
	.end_amdhsa_kernel

amdhsa.kernels:
  - .agpr_count:     0
    .args:
      - .actual_access:  read_only
        .address_space:  global
        .offset:         0
        .size:           8
        .value_kind:     global_buffer
      - .actual_access:  read_only
        .address_space:  global
        .offset:         8
        .size:           8
        .value_kind:     global_buffer
      - .actual_access:  read_only
        .address_space:  global
        .offset:         16
        .size:           8
        .value_kind:     global_buffer
      - .actual_access:  read_only
        .address_space:  global
        .offset:         24
        .size:           8
        .value_kind:     global_buffer
      - .actual_access:  read_only
        .address_space:  global
        .offset:         32
        .size:           8
        .value_kind:     global_buffer
      - .address_space:  global
        .offset:         40
        .size:           8
        .value_kind:     global_buffer
      - .address_space:  global
        .offset:         48
        .size:           8
        .value_kind:     global_buffer
      - .address_space:  global
        .offset:         56
        .size:           8
        .value_kind:     global_buffer
      - .actual_access:  write_only
        .address_space:  global
        .offset:         64
        .size:           8
        .value_kind:     global_buffer
    .group_segment_fixed_size: 0
    .kernarg_segment_align: 8
    .kernarg_segment_size: 72
    .language:       OpenCL C
    .language_version:
      - 2
      - 0
    .max_flat_workgroup_size: 256
    .name:           _Z10cvt_kernelPKfS0_S0_S0_S0_PDF16_S1_S1_P15HIP_vector_typeIfLj2EE
    .private_segment_fixed_size: 0
    .sgpr_count:     30
    .sgpr_spill_count: 0
    .symbol:         _Z10cvt_kernelPKfS0_S0_S0_S0_PDF16_S1_S1_P15HIP_vector_typeIfLj2EE.kd
    .uniform_work_group_size: 1
    .uses_dynamic_stack: false
    .vgpr_count:     21
    .vgpr_spill_count: 0
    .wavefront_size: 64
  - .agpr_count:     0
    .args:
      - .address_space:  global
        .offset:         0
        .size:           8
        .value_kind:     global_buffer
      - .address_space:  global
        .offset:         8
        .size:           8
        .value_kind:     global_buffer
      - .address_space:  global
        .offset:         16
        .size:           8
        .value_kind:     global_buffer
      - .offset:         24
        .size:           4
        .value_kind:     by_value
      - .offset:         28
        .size:           4
        .value_kind:     by_value
      - .offset:         32
        .size:           4
        .value_kind:     by_value
    .group_segment_fixed_size: 0
    .kernarg_segment_align: 8
    .kernarg_segment_size: 36
    .language:       OpenCL C
    .language_version:
      - 2
      - 0
    .max_flat_workgroup_size: 512
    .name:           _Z15gemm_out_kernelPKDF16_S0_Pfiii
    .private_segment_fixed_size: 0
    .sgpr_count:     42
    .sgpr_spill_count: 0
    .symbol:         _Z15gemm_out_kernelPKDF16_S0_Pfiii.kd
    .uniform_work_group_size: 1
    .uses_dynamic_stack: false
    .vgpr_count:     247
    .vgpr_spill_count: 0
    .wavefront_size: 64
  - .agpr_count:     0
    .args:
      - .address_space:  global
        .offset:         0
        .size:           8
        .value_kind:     global_buffer
      - .address_space:  global
        .offset:         8
        .size:           8
        .value_kind:     global_buffer
      - .address_space:  global
        .offset:         16
        .size:           8
        .value_kind:     global_buffer
      - .actual_access:  read_only
        .address_space:  global
        .offset:         24
        .size:           8
        .value_kind:     global_buffer
      - .actual_access:  read_only
        .address_space:  global
        .offset:         32
        .size:           8
        .value_kind:     global_buffer
      - .actual_access:  read_only
        .address_space:  global
        .offset:         40
        .size:           8
        .value_kind:     global_buffer
    .group_segment_fixed_size: 0
    .kernarg_segment_align: 8
    .kernarg_segment_size: 48
    .language:       OpenCL C
    .language_version:
      - 2
      - 0
    .max_flat_workgroup_size: 512
    .name:           _Z15gemm_qkv_kernelPKDF16_S0_PDF16_PKfS3_PK15HIP_vector_typeIfLj2EE
    .private_segment_fixed_size: 0
    .sgpr_count:     78
    .sgpr_spill_count: 0
    .symbol:         _Z15gemm_qkv_kernelPKDF16_S0_PDF16_PKfS3_PK15HIP_vector_typeIfLj2EE.kd
    .uniform_work_group_size: 1
    .uses_dynamic_stack: false
    .vgpr_count:     240
    .vgpr_spill_count: 0
    .wavefront_size: 64
  - .agpr_count:     0
    .args:
      - .actual_access:  read_only
        .address_space:  global
        .offset:         0
        .size:           8
        .value_kind:     global_buffer
      - .actual_access:  write_only
        .address_space:  global
        .offset:         8
        .size:           8
        .value_kind:     global_buffer
      - .offset:         16
        .size:           4
        .value_kind:     hidden_block_count_x
      - .offset:         20
        .size:           4
        .value_kind:     hidden_block_count_y
      - .offset:         24
        .size:           4
        .value_kind:     hidden_block_count_z
      - .offset:         28
        .size:           2
        .value_kind:     hidden_group_size_x
      - .offset:         30
        .size:           2
        .value_kind:     hidden_group_size_y
      - .offset:         32
        .size:           2
        .value_kind:     hidden_group_size_z
      - .offset:         34
        .size:           2
        .value_kind:     hidden_remainder_x
      - .offset:         36
        .size:           2
        .value_kind:     hidden_remainder_y
      - .offset:         38
        .size:           2
        .value_kind:     hidden_remainder_z
      - .offset:         56
        .size:           8
        .value_kind:     hidden_global_offset_x
      - .offset:         64
        .size:           8
        .value_kind:     hidden_global_offset_y
      - .offset:         72
        .size:           8
        .value_kind:     hidden_global_offset_z
      - .offset:         80
        .size:           2
        .value_kind:     hidden_grid_dims
      - .offset:         136
        .size:           4
        .value_kind:     hidden_dynamic_lds_size
    .group_segment_fixed_size: 0
    .kernarg_segment_align: 8
    .kernarg_segment_size: 272
    .language:       OpenCL C
    .language_version:
      - 2
      - 0
    .max_flat_workgroup_size: 512
    .name:           _Z11attn_kernelPKDF16_PDF16_
    .private_segment_fixed_size: 0
    .sgpr_count:     70
    .sgpr_spill_count: 0
    .symbol:         _Z11attn_kernelPKDF16_PDF16_.kd
    .uniform_work_group_size: 1
    .uses_dynamic_stack: false
    .vgpr_count:     256
    .vgpr_spill_count: 0
    .wavefront_size: 64
